# speedup vs baseline: 1.0111x; 1.0109x over previous
.LBB1_9:
.Lqkv_nopoll:
	ds_read_b128 v[130:133], v191
	ds_read_b128 v[134:137], v191 offset:1024
	ds_read_b128 v[138:141], v191 offset:2048
	ds_read_b128 v[142:145], v191 offset:3072
	ds_read_b128 v[146:149], v192
	ds_read_b128 v[150:153], v192 offset:1024
	ds_read_b128 v[154:157], v192 offset:2048
	ds_read_b128 v[158:161], v192 offset:3072
	s_add_u32 s8, s6, 0xfff80080
	s_addc_u32 s9, s7, -1
	s_cmp_eq_u32 s56, 28
	s_cselect_b32 s53, s5, s9
	s_cselect_b32 s52, s10, s8
	s_cselect_b32 s9, s27, s55
	s_cselect_b32 s8, s37, s54
	v_lshl_add_u64 v[184:185], s[6:7], 0, v[176:177]
	s_add_i32 m0, s58, 0xc000
	ds_read_b128 v[200:203], v193
	ds_read_b128 v[204:207], v193 offset:1024
	ds_read_b128 v[208:211], v193 offset:2048
	ds_read_b128 v[212:215], v193 offset:3072
	ds_read_b128 v[216:219], v193 offset:4096
	ds_read_b128 v[220:223], v193 offset:5120
	ds_read_b128 v[224:227], v193 offset:6144
	ds_read_b128 v[228:231], v193 offset:7168
	global_load_lds_dwordx4 v[184:185], off
	v_lshl_add_u64 v[184:185], s[6:7], 0, v[178:179]
	s_add_i32 m0, s58, 0xe000
	s_nop 0
	global_load_lds_dwordx4 v[184:185], off
	s_waitcnt vmcnt(8)
	s_waitcnt lgkmcnt(0)
	s_barrier
	s_setprio 1
	s_waitcnt lgkmcnt(0)
	v_mfma_f32_16x16x32_f16 v[126:129], v[130:133], v[200:203], v[126:129]
	v_mfma_f32_16x16x32_f16 v[122:125], v[138:141], v[200:203], v[122:125]
	v_mfma_f32_16x16x32_f16 v[118:121], v[130:133], v[208:211], v[118:121]
	v_mfma_f32_16x16x32_f16 v[114:117], v[138:141], v[208:211], v[114:117]
	v_mfma_f32_16x16x32_f16 v[102:105], v[130:133], v[216:219], v[102:105]
	v_mfma_f32_16x16x32_f16 v[98:101], v[138:141], v[216:219], v[98:101]
	v_mfma_f32_16x16x32_f16 v[86:89], v[130:133], v[224:227], v[86:89]
	v_mfma_f32_16x16x32_f16 v[82:85], v[138:141], v[224:227], v[82:85]
	v_mfma_f32_16x16x32_f16 v[126:129], v[134:137], v[204:207], v[126:129]
	v_mfma_f32_16x16x32_f16 v[122:125], v[142:145], v[204:207], v[122:125]
	v_mfma_f32_16x16x32_f16 v[118:121], v[134:137], v[212:215], v[118:121]
	v_mfma_f32_16x16x32_f16 v[114:117], v[142:145], v[212:215], v[114:117]
	v_mfma_f32_16x16x32_f16 v[102:105], v[134:137], v[220:223], v[102:105]
	v_mfma_f32_16x16x32_f16 v[98:101], v[142:145], v[220:223], v[98:101]
	v_mfma_f32_16x16x32_f16 v[86:89], v[134:137], v[228:231], v[86:89]
	v_mfma_f32_16x16x32_f16 v[82:85], v[142:145], v[228:231], v[82:85]
	s_setprio 0
	s_setprio 1
	v_mfma_f32_16x16x32_f16 v[110:113], v[146:149], v[200:203], v[110:113]
	v_mfma_f32_16x16x32_f16 v[106:109], v[154:157], v[200:203], v[106:109]
	v_mfma_f32_16x16x32_f16 v[94:97], v[146:149], v[208:211], v[94:97]
	v_mfma_f32_16x16x32_f16 v[90:93], v[154:157], v[208:211], v[90:93]
	v_mfma_f32_16x16x32_f16 v[78:81], v[146:149], v[216:219], v[78:81]
	v_mfma_f32_16x16x32_f16 v[74:77], v[154:157], v[216:219], v[74:77]
	v_mfma_f32_16x16x32_f16 v[70:73], v[146:149], v[224:227], v[70:73]
	v_mfma_f32_16x16x32_f16 v[66:69], v[154:157], v[224:227], v[66:69]
	v_mfma_f32_16x16x32_f16 v[110:113], v[150:153], v[204:207], v[110:113]
	v_mfma_f32_16x16x32_f16 v[106:109], v[158:161], v[204:207], v[106:109]
	v_mfma_f32_16x16x32_f16 v[94:97], v[150:153], v[212:215], v[94:97]
	v_mfma_f32_16x16x32_f16 v[90:93], v[158:161], v[212:215], v[90:93]
	v_mfma_f32_16x16x32_f16 v[78:81], v[150:153], v[220:223], v[78:81]
	v_mfma_f32_16x16x32_f16 v[74:77], v[158:161], v[220:223], v[74:77]
	v_mfma_f32_16x16x32_f16 v[70:73], v[150:153], v[228:231], v[70:73]
	v_mfma_f32_16x16x32_f16 v[66:69], v[158:161], v[228:231], v[66:69]
	s_setprio 0
	s_barrier
	s_add_i32 s57, s68, s3
	v_lshl_add_u64 v[184:185], s[8:9], 0, v[164:165]
	s_mov_b32 m0, s57
	ds_read_b128 v[200:203], v193 offset:16384
	ds_read_b128 v[204:207], v193 offset:17408
	ds_read_b128 v[208:211], v193 offset:18432
	ds_read_b128 v[212:215], v193 offset:19456
	ds_read_b128 v[216:219], v193 offset:20480
	ds_read_b128 v[220:223], v193 offset:21504
	ds_read_b128 v[224:227], v193 offset:22528
	ds_read_b128 v[228:231], v193 offset:23552
	global_load_lds_dwordx4 v[184:185], off
	s_add_i32 m0, s57, 0x2000
	s_add_u32 s78, s8, 0x20000
	v_lshl_add_u64 v[232:233], s[8:9], 0, v[168:169]
	s_addc_u32 s79, s9, 0
	s_add_i32 s57, s69, s3
	global_load_lds_dwordx4 v[232:233], off
	v_lshl_add_u64 v[234:235], s[78:79], 0, v[164:165]
	s_mov_b32 m0, s57
	v_lshl_add_u64 v[236:237], s[52:53], 0, v[166:167]
	global_load_lds_dwordx4 v[234:235], off
	v_lshl_add_u64 v[234:235], s[78:79], 0, v[168:169]
	s_add_i32 m0, s57, 0x2000
	s_nop 0
	global_load_lds_dwordx4 v[234:235], off
	v_lshl_add_u64 v[234:235], s[52:53], 0, v[162:163]
	s_mov_b32 m0, s58
	s_nop 0
	global_load_lds_dwordx4 v[234:235], off
	s_mov_b32 m0, s59
	s_nop 0
	global_load_lds_dwordx4 v[236:237], off
	s_waitcnt vmcnt(8)
	s_waitcnt lgkmcnt(0)
	s_barrier
	s_setprio 1
	s_waitcnt lgkmcnt(0)
	v_mfma_f32_16x16x32_f16 v[62:65], v[130:133], v[200:203], v[62:65]
	v_mfma_f32_16x16x32_f16 v[58:61], v[138:141], v[200:203], v[58:61]
	v_mfma_f32_16x16x32_f16 v[54:57], v[130:133], v[208:211], v[54:57]
	v_mfma_f32_16x16x32_f16 v[50:53], v[138:141], v[208:211], v[50:53]
	v_mfma_f32_16x16x32_f16 v[38:41], v[130:133], v[216:219], v[38:41]
	v_mfma_f32_16x16x32_f16 v[34:37], v[138:141], v[216:219], v[34:37]
	v_mfma_f32_16x16x32_f16 v[22:25], v[130:133], v[224:227], v[22:25]
	v_mfma_f32_16x16x32_f16 v[18:21], v[138:141], v[224:227], v[18:21]
	v_mfma_f32_16x16x32_f16 v[62:65], v[134:137], v[204:207], v[62:65]
	v_mfma_f32_16x16x32_f16 v[58:61], v[142:145], v[204:207], v[58:61]
	v_mfma_f32_16x16x32_f16 v[54:57], v[134:137], v[212:215], v[54:57]
	v_mfma_f32_16x16x32_f16 v[50:53], v[142:145], v[212:215], v[50:53]
	v_mfma_f32_16x16x32_f16 v[38:41], v[134:137], v[220:223], v[38:41]
	v_mfma_f32_16x16x32_f16 v[34:37], v[142:145], v[220:223], v[34:37]
	v_mfma_f32_16x16x32_f16 v[22:25], v[134:137], v[228:231], v[22:25]
	v_mfma_f32_16x16x32_f16 v[18:21], v[142:145], v[228:231], v[18:21]
	s_setprio 0
	s_setprio 1
	v_mfma_f32_16x16x32_f16 v[46:49], v[146:149], v[200:203], v[46:49]
	v_mfma_f32_16x16x32_f16 v[42:45], v[154:157], v[200:203], v[42:45]
	v_mfma_f32_16x16x32_f16 v[30:33], v[146:149], v[208:211], v[30:33]
	v_mfma_f32_16x16x32_f16 v[26:29], v[154:157], v[208:211], v[26:29]
	v_mfma_f32_16x16x32_f16 v[14:17], v[146:149], v[216:219], v[14:17]
	v_mfma_f32_16x16x32_f16 v[10:13], v[154:157], v[216:219], v[10:13]
	v_mfma_f32_16x16x32_f16 v[6:9], v[146:149], v[224:227], v[6:9]
	v_mfma_f32_16x16x32_f16 v[2:5], v[154:157], v[224:227], v[2:5]
	v_mfma_f32_16x16x32_f16 v[46:49], v[150:153], v[204:207], v[46:49]
	v_mfma_f32_16x16x32_f16 v[42:45], v[158:161], v[204:207], v[42:45]
	v_mfma_f32_16x16x32_f16 v[30:33], v[150:153], v[212:215], v[30:33]
	v_mfma_f32_16x16x32_f16 v[26:29], v[158:161], v[212:215], v[26:29]
	v_mfma_f32_16x16x32_f16 v[14:17], v[150:153], v[220:223], v[14:17]
	v_mfma_f32_16x16x32_f16 v[10:13], v[158:161], v[220:223], v[10:13]
	v_mfma_f32_16x16x32_f16 v[6:9], v[150:153], v[228:231], v[6:9]
	v_mfma_f32_16x16x32_f16 v[2:5], v[158:161], v[228:231], v[2:5]
	s_setprio 0
	s_barrier
	s_add_i32 s57, 0, 0x18000
	s_add_i32 s78, 0, 0x1c000
	v_add_u32_e32 v142, s57, v186
	v_add_u32_e32 v158, s78, v186
	ds_read_b128 v[130:133], v142
	ds_read_b128 v[134:137], v142 offset:1024
	ds_read_b128 v[138:141], v142 offset:2048
	ds_read_b128 v[142:145], v142 offset:3072
	ds_read_b128 v[146:149], v158
	ds_read_b128 v[150:153], v158 offset:1024
	ds_read_b128 v[154:157], v158 offset:2048
	ds_read_b128 v[158:161], v158 offset:3072
	s_add_u32 s52, s52, 0x80000
	s_addc_u32 s53, s53, 0
	s_mov_b32 m0, s60
	v_lshl_add_u64 v[238:239], s[52:53], 0, v[162:163]
	ds_read_b128 v[200:203], v193 offset:32768
	ds_read_b128 v[204:207], v193 offset:33792
	ds_read_b128 v[208:211], v193 offset:34816
	ds_read_b128 v[212:215], v193 offset:35840
	ds_read_b128 v[216:219], v193 offset:36864
	ds_read_b128 v[220:223], v193 offset:37888
	ds_read_b128 v[224:227], v193 offset:38912
	ds_read_b128 v[228:231], v193 offset:39936
	global_load_lds_dwordx4 v[238:239], off
	v_lshl_add_u64 v[238:239], s[52:53], 0, v[166:167]
	s_mov_b32 m0, s61
	s_nop 0
	global_load_lds_dwordx4 v[238:239], off
	s_waitcnt vmcnt(8)
	s_waitcnt lgkmcnt(0)
	s_barrier
	s_setprio 1
	s_waitcnt lgkmcnt(0)
	v_mfma_f32_16x16x32_f16 v[126:129], v[130:133], v[200:203], v[126:129]
	v_mfma_f32_16x16x32_f16 v[122:125], v[138:141], v[200:203], v[122:125]
	v_mfma_f32_16x16x32_f16 v[118:121], v[130:133], v[208:211], v[118:121]
	v_mfma_f32_16x16x32_f16 v[114:117], v[138:141], v[208:211], v[114:117]
	v_mfma_f32_16x16x32_f16 v[102:105], v[130:133], v[216:219], v[102:105]
	v_mfma_f32_16x16x32_f16 v[98:101], v[138:141], v[216:219], v[98:101]
	v_mfma_f32_16x16x32_f16 v[86:89], v[130:133], v[224:227], v[86:89]
	v_mfma_f32_16x16x32_f16 v[82:85], v[138:141], v[224:227], v[82:85]
	v_mfma_f32_16x16x32_f16 v[126:129], v[134:137], v[204:207], v[126:129]
	v_mfma_f32_16x16x32_f16 v[122:125], v[142:145], v[204:207], v[122:125]
	v_mfma_f32_16x16x32_f16 v[118:121], v[134:137], v[212:215], v[118:121]
	v_mfma_f32_16x16x32_f16 v[114:117], v[142:145], v[212:215], v[114:117]
	v_mfma_f32_16x16x32_f16 v[102:105], v[134:137], v[220:223], v[102:105]
	v_mfma_f32_16x16x32_f16 v[98:101], v[142:145], v[220:223], v[98:101]
	v_mfma_f32_16x16x32_f16 v[86:89], v[134:137], v[228:231], v[86:89]
	v_mfma_f32_16x16x32_f16 v[82:85], v[142:145], v[228:231], v[82:85]
	s_setprio 0
	s_setprio 1
	v_mfma_f32_16x16x32_f16 v[110:113], v[146:149], v[200:203], v[110:113]
	v_mfma_f32_16x16x32_f16 v[106:109], v[154:157], v[200:203], v[106:109]
	v_mfma_f32_16x16x32_f16 v[94:97], v[146:149], v[208:211], v[94:97]
	v_mfma_f32_16x16x32_f16 v[90:93], v[154:157], v[208:211], v[90:93]
	v_mfma_f32_16x16x32_f16 v[78:81], v[146:149], v[216:219], v[78:81]
	v_mfma_f32_16x16x32_f16 v[74:77], v[154:157], v[216:219], v[74:77]
	v_mfma_f32_16x16x32_f16 v[70:73], v[146:149], v[224:227], v[70:73]
	v_mfma_f32_16x16x32_f16 v[66:69], v[154:157], v[224:227], v[66:69]
	v_mfma_f32_16x16x32_f16 v[110:113], v[150:153], v[204:207], v[110:113]
	v_mfma_f32_16x16x32_f16 v[106:109], v[158:161], v[204:207], v[106:109]
	v_mfma_f32_16x16x32_f16 v[94:97], v[150:153], v[212:215], v[94:97]
	v_mfma_f32_16x16x32_f16 v[90:93], v[158:161], v[212:215], v[90:93]
	v_mfma_f32_16x16x32_f16 v[78:81], v[150:153], v[220:223], v[78:81]
	v_mfma_f32_16x16x32_f16 v[74:77], v[158:161], v[220:223], v[74:77]
	v_mfma_f32_16x16x32_f16 v[70:73], v[150:153], v[228:231], v[70:73]
	v_mfma_f32_16x16x32_f16 v[66:69], v[158:161], v[228:231], v[66:69]
	s_setprio 0
	s_barrier
	s_add_i32 s52, s57, s3
	v_lshl_add_u64 v[184:185], v[184:185], 0, s[44:45]
	s_mov_b32 m0, s52
	ds_read_b128 v[200:203], v193 offset:49152
	ds_read_b128 v[204:207], v193 offset:50176
	ds_read_b128 v[208:211], v193 offset:51200
	ds_read_b128 v[212:215], v193 offset:52224
	ds_read_b128 v[216:219], v193 offset:53248
	ds_read_b128 v[220:223], v193 offset:54272
	ds_read_b128 v[224:227], v193 offset:55296
	ds_read_b128 v[228:231], v193 offset:56320
	global_load_lds_dwordx4 v[184:185], off
	s_add_i32 m0, s52, 0x2000
	s_add_u32 s8, s8, 0x20080
	v_lshl_add_u64 v[184:185], v[232:233], 0, s[44:45]
	s_addc_u32 s9, s9, 0
	s_add_i32 s52, s78, s3
	global_load_lds_dwordx4 v[184:185], off
	v_lshl_add_u64 v[184:185], s[8:9], 0, v[164:165]
	s_mov_b32 m0, s52
	s_nop 0
	global_load_lds_dwordx4 v[184:185], off
	v_lshl_add_u64 v[184:185], s[8:9], 0, v[168:169]
	s_add_i32 m0, s52, 0x2000
	s_nop 0
	global_load_lds_dwordx4 v[184:185], off
	v_lshl_add_u64 v[184:185], v[234:235], 0, s[44:45]
	s_mov_b32 m0, s64
	s_nop 0
	global_load_lds_dwordx4 v[184:185], off
	v_lshl_add_u64 v[184:185], v[236:237], 0, s[44:45]
	s_mov_b32 m0, s65
	s_nop 0
	global_load_lds_dwordx4 v[184:185], off
	s_waitcnt vmcnt(8)
	s_waitcnt lgkmcnt(0)
	s_barrier
	s_setprio 1
	s_waitcnt lgkmcnt(0)
	v_mfma_f32_16x16x32_f16 v[62:65], v[130:133], v[200:203], v[62:65]
	v_mfma_f32_16x16x32_f16 v[58:61], v[138:141], v[200:203], v[58:61]
	v_mfma_f32_16x16x32_f16 v[54:57], v[130:133], v[208:211], v[54:57]
	v_mfma_f32_16x16x32_f16 v[50:53], v[138:141], v[208:211], v[50:53]
	v_mfma_f32_16x16x32_f16 v[38:41], v[130:133], v[216:219], v[38:41]
	v_mfma_f32_16x16x32_f16 v[34:37], v[138:141], v[216:219], v[34:37]
	v_mfma_f32_16x16x32_f16 v[22:25], v[130:133], v[224:227], v[22:25]
	v_mfma_f32_16x16x32_f16 v[18:21], v[138:141], v[224:227], v[18:21]
	v_mfma_f32_16x16x32_f16 v[62:65], v[134:137], v[204:207], v[62:65]
	v_mfma_f32_16x16x32_f16 v[58:61], v[142:145], v[204:207], v[58:61]
	v_mfma_f32_16x16x32_f16 v[54:57], v[134:137], v[212:215], v[54:57]
	v_mfma_f32_16x16x32_f16 v[50:53], v[142:145], v[212:215], v[50:53]
	v_mfma_f32_16x16x32_f16 v[38:41], v[134:137], v[220:223], v[38:41]
	v_mfma_f32_16x16x32_f16 v[34:37], v[142:145], v[220:223], v[34:37]
	v_mfma_f32_16x16x32_f16 v[22:25], v[134:137], v[228:231], v[22:25]
	v_mfma_f32_16x16x32_f16 v[18:21], v[142:145], v[228:231], v[18:21]
	s_setprio 0
	s_setprio 1
	v_mfma_f32_16x16x32_f16 v[46:49], v[146:149], v[200:203], v[46:49]
	v_mfma_f32_16x16x32_f16 v[42:45], v[154:157], v[200:203], v[42:45]
	v_mfma_f32_16x16x32_f16 v[30:33], v[146:149], v[208:211], v[30:33]
	v_mfma_f32_16x16x32_f16 v[26:29], v[154:157], v[208:211], v[26:29]
	v_mfma_f32_16x16x32_f16 v[14:17], v[146:149], v[216:219], v[14:17]
	v_mfma_f32_16x16x32_f16 v[10:13], v[154:157], v[216:219], v[10:13]
	v_mfma_f32_16x16x32_f16 v[6:9], v[146:149], v[224:227], v[6:9]
	v_mfma_f32_16x16x32_f16 v[2:5], v[154:157], v[224:227], v[2:5]
	v_mfma_f32_16x16x32_f16 v[46:49], v[150:153], v[204:207], v[46:49]
	v_mfma_f32_16x16x32_f16 v[42:45], v[158:161], v[204:207], v[42:45]
	v_mfma_f32_16x16x32_f16 v[30:33], v[150:153], v[212:215], v[30:33]
	v_mfma_f32_16x16x32_f16 v[26:29], v[158:161], v[212:215], v[26:29]
	v_mfma_f32_16x16x32_f16 v[14:17], v[150:153], v[220:223], v[14:17]
	v_mfma_f32_16x16x32_f16 v[10:13], v[158:161], v[220:223], v[10:13]
	v_mfma_f32_16x16x32_f16 v[6:9], v[150:153], v[228:231], v[6:9]
	v_mfma_f32_16x16x32_f16 v[2:5], v[158:161], v[228:231], v[2:5]
	s_setprio 0
	s_barrier
	s_add_i32 s56, s56, 2
	s_add_u32 s6, s6, 0x100
	s_addc_u32 s7, s7, 0
	s_add_u32 s54, s54, 0x100
	s_addc_u32 s55, s55, 0
	s_cmp_gt_u32 s56, 29
	s_cbranch_scc0 .LBB1_9
	s_and_b64 vcc, exec, s[46:47]
	s_cbranch_vccz .LBB1_12
	s_barrier
